# non-leader blocks poll top-level barrier generation directly (one hop fewer)
# speedup vs baseline: 1.0023x; 1.0023x over previous
.LBB2_303:
	s_or_b64 exec, exec, s[12:13]
	v_cvt_f32_u32_e32 v6, v4
	s_waitcnt vmcnt(0)
	v_readfirstlane_b32 s10, v5
	v_sub_u32_e32 v5, 0, v4
	v_rcp_iflag_f32_e32 v6, v6
	v_add_u32_e32 v7, s10, v3
	v_mul_f32_e32 v6, 0x4f7ffffe, v6
	v_cvt_u32_f32_e32 v6, v6
	v_mul_lo_u32 v3, v5, v6
	v_mul_hi_u32 v3, v6, v3
	v_add_u32_e32 v3, v6, v3
	v_mul_hi_u32 v3, v7, v3
	v_mul_lo_u32 v5, v3, v4
	v_sub_u32_e32 v5, v7, v5
	v_add_u32_e32 v6, 1, v3
	v_cmp_ge_u32_e32 vcc, v5, v4
	s_nop 1
	v_cndmask_b32_e32 v3, v3, v6, vcc
	v_sub_u32_e32 v6, v5, v4
	v_cndmask_b32_e32 v5, v5, v6, vcc
	v_add_u32_e32 v6, 1, v3
	v_cmp_ge_u32_e32 vcc, v5, v4
	v_add_u32_e32 v5, 1, v7
	s_nop 0
	v_cndmask_b32_e32 v3, v3, v6, vcc
	v_mul_lo_u32 v6, v4, v3
	v_add_u32_e32 v4, v6, v4
	v_cmp_ne_u32_e32 vcc, v5, v4
	s_and_saveexec_b64 s[10:11], vcc
	s_xor_b64 s[10:11], exec, s[10:11]
	s_cbranch_execz .LBB2_317
	s_waitcnt lgkmcnt(0)
	v_mov_b32_e32 v2, 0x3500
	global_load_dword v2, v2, s[54:55] sc1
	s_add_u32 s14, s54, 0x3500
	s_addc_u32 s15, s55, 0
	s_waitcnt vmcnt(0)
	v_cmp_eq_u32_e32 vcc, v2, v3
	s_and_saveexec_b64 s[12:13], vcc
	s_cbranch_execz .LBB2_316
	s_mov_b32 s26, 1
	s_mov_b64 s[16:17], 0
	v_mov_b32_e32 v2, 0
	s_branch .LBB2_307
